# P2 and P9 tile stores non-temporal
# baseline (speedup 1.0000x reference)
.LBB0_3401:
	s_movk_i32 s17, 0x100
	v_mov_b32_e32 v146, v148
	v_mov_b32_e32 v147, v1
	s_nop 0
	v_add_u32_e32 v153, s37, v147
	v_lshlrev_b32_e32 v146, 3, v146
	v_ashrrev_i32_e32 v147, 31, v146
	v_cmp_gt_i32_e32 vcc, s17, v153
	s_and_saveexec_b64 s[24:25], vcc
	s_cbranch_execz .LBB0_3403
	v_add_u32_e32 v154, s6, v153
	v_ashrrev_i32_e32 v155, 31, v154
	v_lshlrev_b64 v[154:155], 12, v[154:155]
	s_lshl_b32 s26, s46, 8
	v_lshl_add_u64 v[154:155], s[96:97], 0, v[154:155]
	s_ashr_i32 s27, s26, 31
	v_lshl_add_u64 v[154:155], s[26:27], 1, v[154:155]
	s_lshl_b32 s8, s38, 1
	v_lshl_add_u64 v[154:155], v[154:155], 0, s[8:9]
	v_lshl_add_u64 v[154:155], v[146:147], 1, v[154:155]
	v_cvt_pk_bf16_f32 v126, v126, v127
	v_cvt_pk_bf16_f32 v127, v128, v129
	v_cvt_pk_bf16_f32 v128, v122, v123
	v_cvt_pk_bf16_f32 v129, v124, v125
	global_store_dwordx4 v[154:155], v[126:129], off nt
	v_cvt_pk_bf16_f32 v118, v118, v119
	v_cvt_pk_bf16_f32 v119, v120, v121
	v_cvt_pk_bf16_f32 v120, v114, v115
	v_cvt_pk_bf16_f32 v121, v116, v117
	global_store_dwordx4 v[154:155], v[118:121], off offset:256 nt
.LBB0_3403:
	s_or_b64 exec, exec, s[24:25]
	v_add_u32_e32 v114, 16, v153
	v_cmp_gt_i32_e32 vcc, s17, v114
	s_and_saveexec_b64 s[24:25], vcc
	s_cbranch_execz .LBB0_3405
	v_add_u32_e32 v114, s6, v114
	v_ashrrev_i32_e32 v115, 31, v114
	v_lshlrev_b64 v[114:115], 12, v[114:115]
	s_lshl_b32 s26, s46, 8
	v_lshl_add_u64 v[114:115], s[96:97], 0, v[114:115]
	s_ashr_i32 s27, s26, 31
	v_lshl_add_u64 v[114:115], s[26:27], 1, v[114:115]
	s_lshl_b32 s8, s38, 1
	v_lshl_add_u64 v[114:115], v[114:115], 0, s[8:9]
	v_lshl_add_u64 v[114:115], v[146:147], 1, v[114:115]
	v_cvt_pk_bf16_f32 v110, v110, v111
	v_cvt_pk_bf16_f32 v111, v112, v113
	v_cvt_pk_bf16_f32 v112, v106, v107
	v_cvt_pk_bf16_f32 v113, v108, v109
	global_store_dwordx4 v[114:115], v[110:113], off nt
	v_cvt_pk_bf16_f32 v102, v102, v103
	v_cvt_pk_bf16_f32 v103, v104, v105
	v_cvt_pk_bf16_f32 v104, v98, v99
	v_cvt_pk_bf16_f32 v105, v100, v101
	global_store_dwordx4 v[114:115], v[102:105], off offset:256 nt
.LBB0_3405:
	s_or_b64 exec, exec, s[24:25]
	v_add_u32_e32 v98, 32, v153
	v_cmp_gt_i32_e32 vcc, s17, v98
	s_and_saveexec_b64 s[24:25], vcc
	s_cbranch_execz .LBB0_3407
	v_add_u32_e32 v98, s6, v98
	v_ashrrev_i32_e32 v99, 31, v98
	v_lshlrev_b64 v[98:99], 12, v[98:99]
	s_lshl_b32 s26, s46, 8
	v_lshl_add_u64 v[98:99], s[96:97], 0, v[98:99]
	s_ashr_i32 s27, s26, 31
	v_lshl_add_u64 v[98:99], s[26:27], 1, v[98:99]
	s_lshl_b32 s8, s38, 1
	v_lshl_add_u64 v[98:99], v[98:99], 0, s[8:9]
	v_lshl_add_u64 v[98:99], v[146:147], 1, v[98:99]
	v_cvt_pk_bf16_f32 v94, v94, v95
	v_cvt_pk_bf16_f32 v95, v96, v97
	v_cvt_pk_bf16_f32 v96, v90, v91
	v_cvt_pk_bf16_f32 v97, v92, v93
	global_store_dwordx4 v[98:99], v[94:97], off nt
	v_cvt_pk_bf16_f32 v86, v86, v87
	v_cvt_pk_bf16_f32 v87, v88, v89
	v_cvt_pk_bf16_f32 v88, v82, v83
	v_cvt_pk_bf16_f32 v89, v84, v85
	global_store_dwordx4 v[98:99], v[86:89], off offset:256 nt
.LBB0_3407:
	s_or_b64 exec, exec, s[24:25]
	v_add_u32_e32 v82, 48, v153
	v_cmp_gt_i32_e32 vcc, s17, v82
	s_and_saveexec_b64 s[24:25], vcc
	s_cbranch_execz .LBB0_3409
	v_add_u32_e32 v82, s6, v82
	v_ashrrev_i32_e32 v83, 31, v82
	v_lshlrev_b64 v[82:83], 12, v[82:83]
	s_lshl_b32 s26, s46, 8
	v_lshl_add_u64 v[82:83], s[96:97], 0, v[82:83]
	s_ashr_i32 s27, s26, 31
	v_lshl_add_u64 v[82:83], s[26:27], 1, v[82:83]
	s_lshl_b32 s8, s38, 1
	v_lshl_add_u64 v[82:83], v[82:83], 0, s[8:9]
	v_lshl_add_u64 v[82:83], v[146:147], 1, v[82:83]
	v_cvt_pk_bf16_f32 v78, v78, v79
	v_cvt_pk_bf16_f32 v79, v80, v81
	v_cvt_pk_bf16_f32 v80, v74, v75
	v_cvt_pk_bf16_f32 v81, v76, v77
	global_store_dwordx4 v[82:83], v[78:81], off nt
	v_cvt_pk_bf16_f32 v70, v70, v71
	v_cvt_pk_bf16_f32 v71, v72, v73
	v_cvt_pk_bf16_f32 v72, v66, v67
	v_cvt_pk_bf16_f32 v73, v68, v69
	global_store_dwordx4 v[82:83], v[70:73], off offset:256 nt
.LBB0_3409:
	s_or_b64 exec, exec, s[24:25]
	v_add_u32_e32 v66, 0x80, v153
	v_cmp_gt_i32_e32 vcc, s17, v66
	s_and_saveexec_b64 s[24:25], vcc
	s_cbranch_execz .LBB0_3411
	v_add_u32_e32 v66, s6, v66
	v_ashrrev_i32_e32 v67, 31, v66
	v_lshlrev_b64 v[66:67], 12, v[66:67]
	s_lshl_b32 s26, s46, 8
	v_lshl_add_u64 v[66:67], s[96:97], 0, v[66:67]
	s_ashr_i32 s27, s26, 31
	v_lshl_add_u64 v[66:67], s[26:27], 1, v[66:67]
	s_lshl_b32 s8, s38, 1
	v_lshl_add_u64 v[66:67], v[66:67], 0, s[8:9]
	v_lshl_add_u64 v[66:67], v[146:147], 1, v[66:67]
	v_cvt_pk_bf16_f32 v62, v62, v63
	v_cvt_pk_bf16_f32 v63, v64, v65
	v_cvt_pk_bf16_f32 v64, v58, v59
	v_cvt_pk_bf16_f32 v65, v60, v61
	global_store_dwordx4 v[66:67], v[62:65], off nt
	v_cvt_pk_bf16_f32 v54, v54, v55
	v_cvt_pk_bf16_f32 v55, v56, v57
	v_cvt_pk_bf16_f32 v56, v50, v51
	v_cvt_pk_bf16_f32 v57, v52, v53
	global_store_dwordx4 v[66:67], v[54:57], off offset:256 nt
.LBB0_3411:
	s_or_b64 exec, exec, s[24:25]
	v_add_u32_e32 v50, 0x90, v153
	v_cmp_gt_i32_e32 vcc, s17, v50
	s_and_saveexec_b64 s[24:25], vcc
	s_cbranch_execz .LBB0_3413
	v_add_u32_e32 v50, s6, v50
	v_ashrrev_i32_e32 v51, 31, v50
	v_lshlrev_b64 v[50:51], 12, v[50:51]
	s_lshl_b32 s26, s46, 8
	v_lshl_add_u64 v[50:51], s[96:97], 0, v[50:51]
	s_ashr_i32 s27, s26, 31
	v_lshl_add_u64 v[50:51], s[26:27], 1, v[50:51]
	s_lshl_b32 s8, s38, 1
	v_lshl_add_u64 v[50:51], v[50:51], 0, s[8:9]
	v_lshl_add_u64 v[50:51], v[146:147], 1, v[50:51]
	v_cvt_pk_bf16_f32 v46, v46, v47
	v_cvt_pk_bf16_f32 v47, v48, v49
	v_cvt_pk_bf16_f32 v48, v42, v43
	v_cvt_pk_bf16_f32 v49, v44, v45
	global_store_dwordx4 v[50:51], v[46:49], off nt
	v_cvt_pk_bf16_f32 v38, v38, v39
	v_cvt_pk_bf16_f32 v39, v40, v41
	v_cvt_pk_bf16_f32 v40, v34, v35
	v_cvt_pk_bf16_f32 v41, v36, v37
	global_store_dwordx4 v[50:51], v[38:41], off offset:256 nt
.LBB0_3413:
	s_or_b64 exec, exec, s[24:25]
	v_add_u32_e32 v34, 0xa0, v153
	v_cmp_gt_i32_e32 vcc, s17, v34
	s_and_saveexec_b64 s[24:25], vcc
	s_cbranch_execz .LBB0_3415
	v_add_u32_e32 v34, s6, v34
	v_ashrrev_i32_e32 v35, 31, v34
	v_lshlrev_b64 v[34:35], 12, v[34:35]
	s_lshl_b32 s26, s46, 8
	v_lshl_add_u64 v[34:35], s[96:97], 0, v[34:35]
	s_ashr_i32 s27, s26, 31
	v_lshl_add_u64 v[34:35], s[26:27], 1, v[34:35]
	s_lshl_b32 s8, s38, 1
	v_lshl_add_u64 v[34:35], v[34:35], 0, s[8:9]
	v_lshl_add_u64 v[34:35], v[146:147], 1, v[34:35]
	v_cvt_pk_bf16_f32 v30, v30, v31
	v_cvt_pk_bf16_f32 v31, v32, v33
	v_cvt_pk_bf16_f32 v32, v26, v27
	v_cvt_pk_bf16_f32 v33, v28, v29
	global_store_dwordx4 v[34:35], v[30:33], off nt
	v_cvt_pk_bf16_f32 v22, v22, v23
	v_cvt_pk_bf16_f32 v23, v24, v25
	v_cvt_pk_bf16_f32 v24, v18, v19
	v_cvt_pk_bf16_f32 v25, v20, v21
	global_store_dwordx4 v[34:35], v[22:25], off offset:256 nt
.LBB0_3415:
	s_or_b64 exec, exec, s[24:25]
	v_add_u32_e32 v18, 0xb0, v153
	v_cmp_gt_i32_e32 vcc, s17, v18
	s_and_saveexec_b64 s[24:25], vcc
	s_cbranch_execz .LBB0_3417
	v_add_u32_e32 v18, s6, v18
	v_ashrrev_i32_e32 v19, 31, v18
	v_lshlrev_b64 v[18:19], 12, v[18:19]
	s_lshl_b32 s26, s46, 8
	v_lshl_add_u64 v[18:19], s[96:97], 0, v[18:19]
	s_ashr_i32 s27, s26, 31
	v_lshl_add_u64 v[18:19], s[26:27], 1, v[18:19]
	s_lshl_b32 s8, s38, 1
	v_lshl_add_u64 v[18:19], v[18:19], 0, s[8:9]
	v_lshl_add_u64 v[18:19], v[146:147], 1, v[18:19]
	v_cvt_pk_bf16_f32 v14, v14, v15
	v_cvt_pk_bf16_f32 v15, v16, v17
	v_cvt_pk_bf16_f32 v16, v10, v11
	v_cvt_pk_bf16_f32 v17, v12, v13
	global_store_dwordx4 v[18:19], v[14:17], off nt
	v_cvt_pk_bf16_f32 v6, v6, v7
	v_cvt_pk_bf16_f32 v7, v8, v9
	v_cvt_pk_bf16_f32 v8, v2, v3
	v_cvt_pk_bf16_f32 v9, v4, v5
	global_store_dwordx4 v[18:19], v[6:9], off offset:256 nt
